# v40 + the same row-top batching of gain/shift/scale loads in norm phase P1
# speedup vs baseline: 1.0149x; 1.0024x over previous
; #define GAS __attribute__((address_space(1)))
; template <bool F8, bool SRCH = false> __device__ __forceinline__ void norm_phase(Frame& F, const float* srcL, const float* srcC, const float* g, const float* mod, int shift_off, int scale_off, int nrows) {
;     ...
;     for (int row = gw; row < nrows; row += NGW) {
;         const float* src = row < ML ? srcL + (size_t)row * DM : srcC + (size_t)(row - ML) * DM;
;         const float* mv = mod + (size_t)(row < ML ? (row >> 13) : 2) * MOD_W;
;         const GAS f32x4* xr = (const GAS f32x4*)src + F.lane;
;         f32x4 v[8]; float s = 0.f;
; #pragma unroll
;         for (int j = 0; j < 8; ++j) {
;             if constexpr (SRCH) { const v2u w = ((const GAS v2u*)(WSP(const bf16, WS_H) + (size_t)row * DM))[F.lane + 64 * j]; v[j].x = bflo(w.x); v[j].y = bfhi(w.x); v[j].z = bflo(w.y); v[j].w = bfhi(w.y); }
;             else v[j] = xr[64 * j];
;             s += (v[j].x * v[j].x + v[j].y * v[j].y) + (v[j].z * v[j].z + v[j].w * v[j].w); }
;         const float rstd = 1.0f / sqrtf(wave_sum(s) * (1.0f / DM) + NORM_EPS);
.LBB0_179:
	global_load_dwordx4 v[30:33], v34, s[14:15]
	global_load_dwordx4 v[26:29], v34, s[14:15] offset:1024
	global_load_dwordx4 v[22:25], v34, s[14:15] offset:2048
	global_load_dwordx4 v[18:21], v34, s[14:15] offset:3072
	v_lshl_add_u64 v[2:3], s[14:15], 0, v[34:35]
	v_add_co_u32_e32 v6, vcc, s20, v2
	s_min_i32 s8, s4, 0x4000
	s_nop 0
	v_addc_co_u32_e32 v7, vcc, 0, v3, vcc
	global_load_dwordx4 v[14:17], v[6:7], off
	global_load_dwordx4 v[10:13], v[6:7], off offset:1024
	global_load_dwordx4 v[2:5], v[6:7], off offset:3072
	s_nop 0
	global_load_dwordx4 v[6:9], v[6:7], off offset:2048
	s_ashr_i32 s8, s8, 13
	s_mul_hi_i32 s15, s8, 0xc000
	s_mul_i32 s8, s8, 0xc000
	s_add_u32 s14, s18, s8
	s_addc_u32 s15, s19, s15
	s_lshl_b64 s[0:1], s[0:1], 12
	s_add_u32 s16, s14, 0x2000
	global_load_dwordx4 v[66:69], v[36:37], off
	s_addc_u32 s17, s15, 0
	global_load_dwordx4 v[70:73], v57, s[14:15]
	global_load_dwordx4 v[74:77], v57, s[16:17]
	global_load_dwordx4 v[98:101], v[36:37], off offset:1024
	global_load_dwordx4 v[102:105], v58, s[16:17]
	global_load_dwordx4 v[106:109], v57, s[14:15] offset:1024
	global_load_dwordx4 v[110:113], v[36:37], off offset:2048
	global_load_dwordx4 v[114:117], v59, s[16:17]
	global_load_dwordx4 v[118:121], v57, s[14:15] offset:2048
	global_load_dwordx4 v[122:125], v[36:37], off offset:3072
	global_load_dwordx4 v[126:129], v60, s[16:17]
	global_load_dwordx4 v[130:133], v57, s[14:15] offset:3072
	global_load_dwordx4 v[134:137], v[38:39], off
	global_load_dwordx4 v[138:141], v61, s[16:17]
	global_load_dwordx4 v[142:145], v61, s[14:15]
	global_load_dwordx4 v[146:149], v[40:41], off
	global_load_dwordx4 v[150:153], v62, s[16:17]
	global_load_dwordx4 v[154:157], v62, s[14:15]
	global_load_dwordx4 v[158:161], v[42:43], off
	global_load_dwordx4 v[162:165], v63, s[16:17]
	global_load_dwordx4 v[166:169], v63, s[14:15]
	global_load_dwordx4 v[170:173], v[44:45], off
	global_load_dwordx4 v[174:177], v64, s[16:17]
	global_load_dwordx4 v[182:185], v64, s[14:15]
	s_add_u32 s4, s4, s6
	s_addc_u32 s5, s5, s7
	s_add_u32 s10, s10, s12
	s_addc_u32 s11, s11, s13
	s_cmpk_lt_i32 s4, 0x4200
	s_waitcnt vmcnt(31)
	v_mov_b32_e32 v78, v31
	s_waitcnt vmcnt(30)
	v_mov_b32_e32 v79, v27
	v_mov_b32_e32 v82, v33
	v_mov_b32_e32 v83, v29
	v_mov_b32_e32 v48, v30
	v_mov_b32_e32 v49, v26
	v_mov_b32_e32 v80, v32
	v_mov_b32_e32 v81, v28
	s_waitcnt vmcnt(29)
	v_pk_mul_f32 v[84:85], v[24:25], v[24:25]
	v_pk_mul_f32 v[86:87], v[22:23], v[22:23]
	v_pk_mul_f32 v[78:79], v[78:79], v[78:79]
	v_pk_mul_f32 v[82:83], v[82:83], v[82:83]
	v_pk_mov_b32 v[92:93], v[86:87], v[84:85] op_sel:[1,0]
	v_mov_b32_e32 v87, v85
	v_pk_fma_f32 v[48:49], v[48:49], v[48:49], v[78:79]
	v_pk_fma_f32 v[78:79], v[80:81], v[80:81], v[82:83]
	s_waitcnt vmcnt(28)
	v_mul_f32_e32 v88, v19, v19
	v_mul_f32_e32 v90, v21, v21
	v_pk_add_f32 v[80:81], v[92:93], v[86:87]
	v_pk_add_f32 v[48:49], v[48:49], v[78:79]
	v_pk_fma_f32 v[84:85], v[18:19], v[18:19], v[88:89] op_sel_hi:[1,1,0]
	v_pk_fma_f32 v[88:89], v[20:21], v[20:21], v[90:91] op_sel_hi:[1,1,0]
	s_waitcnt vmcnt(27)
	v_mul_f32_e32 v65, v14, v14
	v_mul_f32_e32 v93, v15, v15
	v_pk_add_f32 v[78:79], v[80:81], v[80:81] op_sel:[0,1] op_sel_hi:[1,0]
	v_pk_add_f32 v[48:49], v[48:49], v[48:49] op_sel:[0,1] op_sel_hi:[1,0]
	v_mul_f32_e32 v85, v16, v16
	v_mul_f32_e32 v89, v17, v17
	s_waitcnt vmcnt(26)
	v_pk_mul_f32 v[82:83], v[12:13], v[12:13]
	v_pk_mul_f32 v[86:87], v[10:11], v[10:11]
	v_mov_b32_e32 v79, v93
	v_mov_b32_e32 v49, v65
	v_pk_mov_b32 v[80:81], v[86:87], v[82:83] op_sel:[1,0]
	v_mov_b32_e32 v87, v83
	v_pk_add_f32 v[84:85], v[84:85], v[88:89]
	v_pk_add_f32 v[48:49], v[48:49], v[78:79]
	s_waitcnt vmcnt(24)
	v_mul_f32_e32 v90, v7, v7
	v_mul_f32_e32 v92, v9, v9
	v_pk_add_f32 v[80:81], v[80:81], v[86:87]
	v_pk_add_f32 v[48:49], v[48:49], v[84:85]
	v_mul_f32_e32 v94, v2, v2
	v_mul_f32_e32 v95, v3, v3
	v_mul_f32_e32 v96, v4, v4
	v_mul_f32_e32 v97, v5, v5
	v_pk_fma_f32 v[82:83], v[6:7], v[6:7], v[90:91] op_sel_hi:[1,1,0]
	v_pk_fma_f32 v[90:91], v[8:9], v[8:9], v[92:93] op_sel_hi:[1,1,0]
	v_pk_add_f32 v[80:81], v[80:81], v[80:81] op_sel:[0,1] op_sel_hi:[1,0]
	v_pk_add_f32 v[48:49], v[48:49], v[48:49] op_sel:[0,1] op_sel_hi:[1,0]
	v_mov_b32_e32 v83, v96
	v_mov_b32_e32 v91, v97
	v_mov_b32_e32 v81, v95
	v_mov_b32_e32 v49, v94
	v_pk_add_f32 v[82:83], v[82:83], v[90:91]
	v_pk_add_f32 v[48:49], v[48:49], v[80:81]
	s_waitcnt vmcnt(0)
	v_pk_add_f32 v[74:75], v[74:75], 1.0 op_sel_hi:[1,0]
	v_pk_add_f32 v[48:49], v[48:49], v[82:83]
	v_pk_add_f32 v[76:77], v[76:77], 1.0 op_sel_hi:[1,0]
	v_add_f32_e32 v48, v48, v49
	ds_bpermute_b32 v49, v1, v48
	s_waitcnt lgkmcnt(0)
	v_add_f32_e32 v48, v48, v49
	ds_bpermute_b32 v49, v50, v48
	s_waitcnt lgkmcnt(0)
	v_add_f32_e32 v48, v48, v49
	ds_bpermute_b32 v49, v51, v48
	s_waitcnt lgkmcnt(0)
	v_add_f32_e32 v48, v48, v49
	ds_bpermute_b32 v49, v52, v48
	s_waitcnt lgkmcnt(0)
	v_add_f32_e32 v48, v48, v49
	ds_bpermute_b32 v49, v53, v48
	s_waitcnt lgkmcnt(0)
	v_add_f32_e32 v48, v48, v49
	ds_bpermute_b32 v49, v54, v48
	s_waitcnt lgkmcnt(0)
; #define GAS __attribute__((address_space(1)))
; __device__ __forceinline__ unsigned pk2(float lo, float hi) { return pg8::cvt_pk_bf16(lo, hi); }
; __device__ __forceinline__ unsigned pk4_fp8(float a, float b, float c, float d) { int p = 0; p = __builtin_amdgcn_cvt_pk_fp8_f32(a, b, p, false); p = __builtin_amdgcn_cvt_pk_fp8_f32(c, d, p, true); return (unsigned)p; }
; __device__ __forceinline__ float clamp8(float x) { return __builtin_fminf(__builtin_fmaxf(x, -448.0f), 448.0f); }
; template <bool F8, bool SRCH = false> __device__ __forceinline__ void norm_phase(Frame& F, const float* srcL, const float* srcC, const float* g, const float* mod, int shift_off, int scale_off, int nrows) {
;     ...
;         const float rstd = 1.0f / sqrtf(wave_sum(s) * (1.0f / DM) + NORM_EPS);
;         GAS v2u* o8 = (GAS v2u*)(XN + (size_t)row * DM) + F.lane;
; #pragma unroll
;         for (int j = 0; j < 8; ++j) { const int col = 4 * (F.lane + 64 * j);
;             const f32x4 gg = *(const GAS f32x4*)(g + col), sh = *(const GAS f32x4*)(mv + shift_off + col), sc = *(const GAS f32x4*)(mv + scale_off + col);
;             const f32x4 y = v[j] * rstd * gg * (sc + 1.0f) + sh;
;             if (F8) { ((GAS unsigned*)((unsigned char*)XN + (size_t)row * DM))[F.lane + 64 * j] = pk4_fp8(clamp8(y.x), clamp8(y.y), clamp8(y.z), clamp8(y.w)); }
;             else { v2u w; w.x = pk2(y.x, y.y); w.y = pk2(y.z, y.w); o8[64 * j] = w; } }
	v_add_f32_e32 v48, v48, v49
	v_fmamk_f32 v48, v48, 0x3a000000, v55
	v_mul_f32_e32 v49, 0x4f800000, v48
	v_cmp_gt_f32_e32 vcc, s21, v48
	s_nop 1
	v_cndmask_b32_e32 v65, v48, v49, vcc
	v_sqrt_f32_e32 v78, v65
	v_lshl_add_u64 v[48:49], v[46:47], 0, s[0:1]
	v_add_u32_e32 v79, -1, v78
	v_add_u32_e32 v80, 1, v78
	v_fma_f32 v81, -v79, v78, v65
	v_fma_f32 v82, -v80, v78, v65
	v_cmp_ge_f32_e64 s[0:1], 0, v81
	s_nop 1
	v_cndmask_b32_e64 v78, v78, v79, s[0:1]
	v_cmp_lt_f32_e64 s[0:1], 0, v82
	s_nop 1
	v_cndmask_b32_e64 v78, v78, v80, s[0:1]
	v_mul_f32_e32 v79, 0x37800000, v78
	v_cndmask_b32_e32 v78, v78, v79, vcc
	v_cmp_class_f32_e32 vcc, v65, v56
	s_nop 1
	v_cndmask_b32_e32 v65, v78, v65, vcc
	v_div_scale_f32 v78, s[0:1], v65, v65, 1.0
	v_rcp_f32_e32 v79, v78
	v_div_scale_f32 v80, vcc, 1.0, v65, 1.0
	v_fma_f32 v81, -v78, v79, 1.0
	v_fmac_f32_e32 v79, v81, v79
	v_mul_f32_e32 v81, v80, v79
	v_fma_f32 v82, -v78, v81, v80
	v_fmac_f32_e32 v81, v82, v79
	v_fma_f32 v78, -v78, v81, v80
	v_div_fmas_f32 v78, v78, v79, v81
	v_div_fixup_f32 v78, v78, v65, 1.0
	v_pk_mul_f32 v[30:31], v[30:31], v[78:79] op_sel_hi:[1,0]
	v_pk_mul_f32 v[32:33], v[32:33], v[78:79] op_sel_hi:[1,0]
	v_pk_mul_f32 v[30:31], v[66:67], v[30:31]
	v_pk_mul_f32 v[32:33], v[68:69], v[32:33]
	v_pk_fma_f32 v[30:31], v[74:75], v[30:31], v[70:71]
	v_pk_fma_f32 v[32:33], v[76:77], v[32:33], v[72:73]
	v_cvt_pk_bf16_f32 v30, v30, v31
	v_pk_mul_f32 v[28:29], v[28:29], v[78:79] op_sel_hi:[1,0]
	v_cvt_pk_bf16_f32 v31, v32, v33
	global_store_dwordx2 v[48:49], v[30:31], off
	v_mov_b32_e32 v30, v98
	v_mov_b32_e32 v31, v99
	v_mov_b32_e32 v32, v100
	v_mov_b32_e32 v33, v101
	s_nop 0
	v_mov_b32_e32 v66, v102
	v_mov_b32_e32 v67, v103
	v_mov_b32_e32 v68, v104
	v_mov_b32_e32 v69, v105
	v_mov_b32_e32 v70, v106
	v_mov_b32_e32 v71, v107
	v_mov_b32_e32 v72, v108
	v_mov_b32_e32 v73, v109
	v_pk_mul_f32 v[26:27], v[26:27], v[78:79] op_sel_hi:[1,0]
	v_pk_mul_f32 v[24:25], v[24:25], v[78:79] op_sel_hi:[1,0]
	v_pk_mul_f32 v[22:23], v[22:23], v[78:79] op_sel_hi:[1,0]
	v_pk_mul_f32 v[20:21], v[20:21], v[78:79] op_sel_hi:[1,0]
	v_pk_mul_f32 v[18:19], v[18:19], v[78:79] op_sel_hi:[1,0]
	v_pk_mul_f32 v[16:17], v[16:17], v[78:79] op_sel_hi:[1,0]
	v_pk_mul_f32 v[14:15], v[14:15], v[78:79] op_sel_hi:[1,0]
	v_pk_mul_f32 v[12:13], v[12:13], v[78:79] op_sel_hi:[1,0]
	v_pk_mul_f32 v[10:11], v[10:11], v[78:79] op_sel_hi:[1,0]
	v_pk_mul_f32 v[8:9], v[8:9], v[78:79] op_sel_hi:[1,0]
	v_pk_mul_f32 v[6:7], v[6:7], v[78:79] op_sel_hi:[1,0]
	v_pk_mul_f32 v[4:5], v[4:5], v[78:79] op_sel_hi:[1,0]
	v_pk_mul_f32 v[2:3], v[2:3], v[78:79] op_sel_hi:[1,0]
	v_pk_mul_f32 v[26:27], v[30:31], v[26:27]
	v_pk_mul_f32 v[28:29], v[32:33], v[28:29]
	v_pk_add_f32 v[32:33], v[66:67], 1.0 op_sel_hi:[1,0]
	v_pk_add_f32 v[30:31], v[68:69], 1.0 op_sel_hi:[1,0]
	v_pk_fma_f32 v[26:27], v[32:33], v[26:27], v[70:71]
	v_pk_fma_f32 v[28:29], v[30:31], v[28:29], v[72:73]
	v_cvt_pk_bf16_f32 v26, v26, v27
	s_nop 0
	v_cvt_pk_bf16_f32 v27, v28, v29
	global_store_dwordx2 v[48:49], v[26:27], off offset:512
	v_mov_b32_e32 v26, v110
	v_mov_b32_e32 v27, v111
	v_mov_b32_e32 v28, v112
	v_mov_b32_e32 v29, v113
	s_nop 0
	v_mov_b32_e32 v30, v114
	v_mov_b32_e32 v31, v115
	v_mov_b32_e32 v32, v116
	v_mov_b32_e32 v33, v117
	v_mov_b32_e32 v66, v118
	v_mov_b32_e32 v67, v119
	v_mov_b32_e32 v68, v120
	v_mov_b32_e32 v69, v121
	v_pk_mul_f32 v[22:23], v[22:23], v[26:27]
	v_pk_mul_f32 v[24:25], v[24:25], v[28:29]
	v_pk_add_f32 v[28:29], v[30:31], 1.0 op_sel_hi:[1,0]
	v_pk_add_f32 v[26:27], v[32:33], 1.0 op_sel_hi:[1,0]
	v_pk_fma_f32 v[22:23], v[22:23], v[28:29], v[66:67]
	v_pk_fma_f32 v[24:25], v[24:25], v[26:27], v[68:69]
	v_cvt_pk_bf16_f32 v22, v22, v23
	s_nop 0
	v_cvt_pk_bf16_f32 v23, v24, v25
; #define GAS __attribute__((address_space(1)))
; __device__ __forceinline__ unsigned pk2(float lo, float hi) { return pg8::cvt_pk_bf16(lo, hi); }
; __device__ __forceinline__ unsigned pk4_fp8(float a, float b, float c, float d) { int p = 0; p = __builtin_amdgcn_cvt_pk_fp8_f32(a, b, p, false); p = __builtin_amdgcn_cvt_pk_fp8_f32(c, d, p, true); return (unsigned)p; }
; __device__ __forceinline__ float clamp8(float x) { return __builtin_fminf(__builtin_fmaxf(x, -448.0f), 448.0f); }
; template <bool F8, bool SRCH = false> __device__ __forceinline__ void norm_phase(Frame& F, const float* srcL, const float* srcC, const float* g, const float* mod, int shift_off, int scale_off, int nrows) {
;     ...
; #pragma unroll
;         for (int j = 0; j < 8; ++j) { const int col = 4 * (F.lane + 64 * j);
;             const f32x4 gg = *(const GAS f32x4*)(g + col), sh = *(const GAS f32x4*)(mv + shift_off + col), sc = *(const GAS f32x4*)(mv + scale_off + col);
;             const f32x4 y = v[j] * rstd * gg * (sc + 1.0f) + sh;
;             if (F8) { ((GAS unsigned*)((unsigned char*)XN + (size_t)row * DM))[F.lane + 64 * j] = pk4_fp8(clamp8(y.x), clamp8(y.y), clamp8(y.z), clamp8(y.w)); }
;             else { v2u w; w.x = pk2(y.x, y.y); w.y = pk2(y.z, y.w); o8[64 * j] = w; } }
	global_store_dwordx2 v[48:49], v[22:23], off offset:1024
	v_mov_b32_e32 v22, v122
	v_mov_b32_e32 v23, v123
	v_mov_b32_e32 v24, v124
	v_mov_b32_e32 v25, v125
	s_nop 0
	v_mov_b32_e32 v26, v126
	v_mov_b32_e32 v27, v127
	v_mov_b32_e32 v28, v128
	v_mov_b32_e32 v29, v129
	v_mov_b32_e32 v30, v130
	v_mov_b32_e32 v31, v131
	v_mov_b32_e32 v32, v132
	v_mov_b32_e32 v33, v133
	v_pk_mul_f32 v[18:19], v[18:19], v[22:23]
	v_pk_mul_f32 v[20:21], v[20:21], v[24:25]
	v_pk_add_f32 v[24:25], v[26:27], 1.0 op_sel_hi:[1,0]
	v_pk_add_f32 v[22:23], v[28:29], 1.0 op_sel_hi:[1,0]
	v_pk_fma_f32 v[18:19], v[18:19], v[24:25], v[30:31]
	v_pk_fma_f32 v[20:21], v[20:21], v[22:23], v[32:33]
	v_cvt_pk_bf16_f32 v18, v18, v19
	s_nop 0
	v_cvt_pk_bf16_f32 v19, v20, v21
	global_store_dwordx2 v[48:49], v[18:19], off offset:1536
	v_mov_b32_e32 v18, v134
	v_mov_b32_e32 v19, v135
	v_mov_b32_e32 v20, v136
	v_mov_b32_e32 v21, v137
	s_nop 0
	v_mov_b32_e32 v22, v138
	v_mov_b32_e32 v23, v139
	v_mov_b32_e32 v24, v140
	v_mov_b32_e32 v25, v141
	v_mov_b32_e32 v26, v142
	v_mov_b32_e32 v27, v143
	v_mov_b32_e32 v28, v144
	v_mov_b32_e32 v29, v145
	v_pk_mul_f32 v[14:15], v[14:15], v[18:19]
	v_pk_mul_f32 v[16:17], v[16:17], v[20:21]
	v_pk_add_f32 v[20:21], v[22:23], 1.0 op_sel_hi:[1,0]
	v_pk_add_f32 v[18:19], v[24:25], 1.0 op_sel_hi:[1,0]
	v_pk_fma_f32 v[14:15], v[14:15], v[20:21], v[26:27]
	v_pk_fma_f32 v[16:17], v[16:17], v[18:19], v[28:29]
	v_cvt_pk_bf16_f32 v14, v14, v15
	s_nop 0
	v_cvt_pk_bf16_f32 v15, v16, v17
	global_store_dwordx2 v[48:49], v[14:15], off offset:2048
	v_mov_b32_e32 v14, v146
	v_mov_b32_e32 v15, v147
	v_mov_b32_e32 v16, v148
	v_mov_b32_e32 v17, v149
	s_nop 0
	v_mov_b32_e32 v18, v150
	v_mov_b32_e32 v19, v151
	v_mov_b32_e32 v20, v152
	v_mov_b32_e32 v21, v153
	v_mov_b32_e32 v22, v154
	v_mov_b32_e32 v23, v155
	v_mov_b32_e32 v24, v156
	v_mov_b32_e32 v25, v157
	v_pk_mul_f32 v[10:11], v[10:11], v[14:15]
	v_pk_mul_f32 v[12:13], v[12:13], v[16:17]
	v_pk_add_f32 v[16:17], v[18:19], 1.0 op_sel_hi:[1,0]
	v_pk_add_f32 v[14:15], v[20:21], 1.0 op_sel_hi:[1,0]
	v_pk_fma_f32 v[10:11], v[10:11], v[16:17], v[22:23]
	v_pk_fma_f32 v[12:13], v[12:13], v[14:15], v[24:25]
	v_cvt_pk_bf16_f32 v10, v10, v11
	s_nop 0
	v_cvt_pk_bf16_f32 v11, v12, v13
	global_store_dwordx2 v[48:49], v[10:11], off offset:2560
	v_mov_b32_e32 v10, v158
	v_mov_b32_e32 v11, v159
	v_mov_b32_e32 v12, v160
	v_mov_b32_e32 v13, v161
	s_nop 0
	v_mov_b32_e32 v14, v162
	v_mov_b32_e32 v15, v163
	v_mov_b32_e32 v16, v164
	v_mov_b32_e32 v17, v165
	v_mov_b32_e32 v18, v166
	v_mov_b32_e32 v19, v167
	v_mov_b32_e32 v20, v168
	v_mov_b32_e32 v21, v169
	v_pk_mul_f32 v[6:7], v[6:7], v[10:11]
	v_pk_mul_f32 v[8:9], v[8:9], v[12:13]
	v_pk_add_f32 v[12:13], v[14:15], 1.0 op_sel_hi:[1,0]
	v_pk_add_f32 v[10:11], v[16:17], 1.0 op_sel_hi:[1,0]
	v_pk_fma_f32 v[6:7], v[6:7], v[12:13], v[18:19]
	v_pk_fma_f32 v[8:9], v[8:9], v[10:11], v[20:21]
	v_cvt_pk_bf16_f32 v6, v6, v7
	s_nop 0
	v_cvt_pk_bf16_f32 v7, v8, v9
	global_store_dwordx2 v[48:49], v[6:7], off offset:3072
	v_mov_b32_e32 v6, v170
	v_mov_b32_e32 v7, v171
	v_mov_b32_e32 v8, v172
	v_mov_b32_e32 v9, v173
	s_nop 0
	v_mov_b32_e32 v10, v174
	v_mov_b32_e32 v11, v175
	v_mov_b32_e32 v12, v176
	v_mov_b32_e32 v13, v177
	v_mov_b32_e32 v14, v182
	v_mov_b32_e32 v15, v183
	v_mov_b32_e32 v16, v184
	v_mov_b32_e32 v17, v185
	v_pk_mul_f32 v[2:3], v[2:3], v[6:7]
	v_pk_mul_f32 v[4:5], v[4:5], v[8:9]
	v_pk_add_f32 v[8:9], v[10:11], 1.0 op_sel_hi:[1,0]
	v_pk_add_f32 v[6:7], v[12:13], 1.0 op_sel_hi:[1,0]
	v_pk_fma_f32 v[2:3], v[2:3], v[8:9], v[14:15]
	v_pk_fma_f32 v[4:5], v[4:5], v[6:7], v[16:17]
	v_cvt_pk_bf16_f32 v2, v2, v3
	s_nop 0
	v_cvt_pk_bf16_f32 v3, v4, v5
	global_store_dwordx2 v[48:49], v[2:3], off offset:3584
	s_cbranch_scc0 .LBB0_182
